# phase D: C_prev, value-row and gate loads hoisted to the top of each unit (on top of the phase-F DPP rewrite)
# baseline (speedup 1.0000x reference)
.LBB0_575:
	s_waitcnt lgkmcnt(0)
	s_add_u32 s10, s76, 0x3e200000
	s_addc_u32 s11, s77, 0
	s_and_b32 s21, s19, 3
	s_lshl_b32 s22, s21, 13
	s_lshl_b32 s23, s18, 7
	s_or_b32 s20, s22, s23
	s_add_u32 s14, s76, 0x32000000
	v_and_b32_e32 v106, 15, v175
	s_addc_u32 s15, s77, 0
	s_mul_i32 s3, s74, 0x1200
	v_lshl_or_b32 v176, s57, 4, v106
	s_add_u32 s12, s4, s3
	s_mul_hi_u32 s3, s74, 0x1200
	v_add_u32_e32 v142, s20, v176
	v_mov_b64_e32 v[2:3], s[10:11]
	s_addc_u32 s13, s5, s3
	v_mad_i64_i32 v[2:3], s[4:5], v142, s67, v[2:3]
	s_lshl_b32 s40, s16, 1
	v_lshl_add_u64 v[2:3], v[2:3], 0, s[40:41]
	s_mul_i32 s40, s97, 0x60
	s_lshl_b32 s4, s40, 1
	s_add_u32 s6, s0, s6
	s_addc_u32 s7, s1, s7
	s_load_dwordx2 s[6:7], s[6:7], 0x0
	s_mov_b32 s5, s41
	s_mul_i32 s3, s74, 0x600
	v_lshl_add_u64 v[2:3], v[2:3], 0, s[4:5]
	s_mul_hi_u32 s4, s74, 0x600
	s_waitcnt lgkmcnt(0)
	s_add_u32 s3, s6, s3
	s_addc_u32 s5, s7, s4
	s_lshl_b32 s4, s40, 2
	v_lshlrev_b32_e32 v144, 2, v177
	s_add_u32 s4, s3, s4
	v_ashrrev_i32_e32 v145, 31, v144
	s_addc_u32 s5, s5, 0
	v_lshl_add_u64 v[2:3], v[144:145], 1, v[2:3]
	v_lshl_add_u64 v[4:5], v[144:145], 2, s[4:5]
	global_load_dwordx4 v[22:25], v[4:5], off
	global_load_dwordx4 v[18:21], v[4:5], off offset:64
	global_load_dwordx2 v[156:157], v[2:3], off
	global_load_dwordx2 v[154:155], v[2:3], off offset:32
	global_load_dwordx2 v[152:153], v[2:3], off offset:64
	global_load_dwordx2 v[150:151], v[2:3], off offset:96
	global_load_dwordx4 v[14:17], v[4:5], off offset:128
	global_load_dwordx4 v[10:13], v[4:5], off offset:192
	global_load_dwordx2 v[148:149], v[2:3], off offset:128
	global_load_dwordx2 v[146:147], v[2:3], off offset:160
	global_load_dwordx4 v[6:9], v[4:5], off offset:256
	s_nop 0
	global_load_dwordx4 v[2:5], v[4:5], off offset:320
	s_lshl_b32 s62, s21, 2
	s_add_i32 s62, s62, s97
	s_lshl_b32 s62, s62, 7
	s_add_i32 s62, s62, s18
	s_mul_i32 s62, s62, 0x2400
	s_lshr_b32 s63, s75, 10
	s_lshl_b32 s63, s63, 25
	s_add_u32 s60, s76, 0x65200000
	s_addc_u32 s61, s77, 0
	s_add_u32 s60, s60, s63
	s_addc_u32 s61, s61, 0
	s_add_u32 s60, s60, s62
	s_addc_u32 s61, s61, 0
	s_cmp_lg_u32 s57, 0
	s_cselect_b32 s63, 0x8dc00, 0
	s_add_i32 s63, s63, 0x2000
	v_lshlrev_b32_e32 v120, 4, v80
	global_load_dwordx4 v[108:111], v120, s[60:61]
	v_add_u32_e32 v121, s63, v120
	global_load_dwordx4 v[112:115], v121, s[60:61]
	v_add_u32_e32 v121, 0x91c00, v120
	global_load_dwordx4 v[116:119], v121, s[60:61]
	s_mul_i32 s96, s20, 0x1400
	s_lshr_b32 s87, s75, 10
	s_mul_i32 s87, s87, 0x920
	s_mul_i32 s88, s97, 0xc0
	s_add_i32 s87, s87, s88
	s_add_i32 s87, s87, 0x300
	s_add_u32 s92, s76, 0x3e200000
	s_addc_u32 s93, s77, 0
	s_add_u32 s92, s92, s96
	s_addc_u32 s93, s93, 0
	s_add_u32 s92, s92, s87
	s_addc_u32 s93, s93, 0
	v_mul_u32_u24_e32 v121, 0xaaab, v80
	v_lshrrev_b32_e32 v121, 19, v121
	v_mul_u32_u24_e32 v121, 0x1340, v121
	v_lshl_add_u32 v121, v80, 4, v121
	global_load_dwordx4 v[122:125], v121, s[92:93]
	v_add_u32_e32 v120, 0x200, v80
	v_mul_u32_u24_e32 v121, 0xaaab, v120
	v_lshrrev_b32_e32 v121, 19, v121
	v_mul_u32_u24_e32 v121, 0x1340, v121
	v_lshl_add_u32 v121, v120, 4, v121
	global_load_dwordx4 v[126:129], v121, s[92:93]
	v_add_u32_e32 v120, 0x400, v80
	v_mul_u32_u24_e32 v121, 0xaaab, v120
	v_lshrrev_b32_e32 v121, 19, v121
	v_mul_u32_u24_e32 v121, 0x1340, v121
	v_lshl_add_u32 v121, v120, 4, v121
	global_load_dwordx4 v[130:133], v121, s[92:93]
	s_cmpk_gt_u32 s75, 0x3ff
	s_cbranch_scc1 .Lhoist_D_nogates
	s_lshl_b32 s87, s97, 1
	s_add_i32 s87, s87, 0x900
	s_add_u32 s92, s76, 0x3e200000
	s_addc_u32 s93, s77, 0
	s_add_u32 s92, s92, s96
	s_addc_u32 s93, s93, 0
	s_add_u32 s92, s92, s87
	s_addc_u32 s93, s93, 0
	v_mul_u32_u24_e32 v120, 0x2800, v175
	v_add_u32_e32 v121, 0x1400, v120
	global_load_ushort v138, v120, s[92:93] offset:8
	global_load_ushort v139, v120, s[92:93] offset:24
	global_load_ushort v140, v121, s[92:93] offset:8
	global_load_ushort v141, v121, s[92:93] offset:24
	global_load_ushort v182, v121, s[92:93]
	global_load_ushort v183, v121, s[92:93] offset:16
	global_load_ushort v184, v120, s[92:93] offset:16
	global_load_ushort v185, v120, s[92:93]
	s_lshl_b32 s87, s21, 2
	s_add_i32 s87, s87, s97
	s_lshl_b32 s87, s87, 7
	s_add_i32 s87, s87, s18
	s_lshl_b32 s87, s87, 2
	s_add_u32 s92, s76, 0x99204000
	s_addc_u32 s93, s77, 0
	s_add_u32 s92, s92, s87
	s_addc_u32 s93, s93, 0
	global_load_dword v186, v215, s[92:93]
	global_load_dword v187, v215, s[92:93] offset:256
.Lhoist_D_nogates:
	v_mul_hi_i32 v50, v80, s86
	v_lshrrev_b32_e32 v51, 31, v50
	v_ashrrev_i32_e32 v50, 1, v50
	v_add_u32_e32 v81, v50, v51
	v_mul_lo_u32 v50, v81, 12
	v_sub_u32_e32 v82, v80, v50
	v_add_u32_e32 v50, -6, v82
	v_cmp_lt_i32_e64 s[4:5], 5, v82
	v_add_u32_e32 v70, s23, v81
	s_mul_i32 s3, s97, 48
	v_cndmask_b32_e64 v83, v82, v50, s[4:5]
	s_mov_b64 s[6:7], -1
	s_and_b64 vcc, exec, s[78:79]
	v_add_u32_e32 v59, s22, v70
	v_lshlrev_b32_e32 v56, 3, v83
	s_cbranch_vccz .LBB0_577
	v_mov_b64_e32 v[50:51], s[10:11]
	v_mad_i64_i32 v[50:51], s[6:7], v59, s67, v[50:51]
	v_cndmask_b32_e64 v214, v235, v197, s[4:5]
	v_lshl_add_u64 v[50:51], v[50:51], 0, v[214:215]
	s_lshl_b32 s6, s3, 1
	s_mov_b32 s7, s41
	v_mul_lo_u32 v54, v70, 24
	v_lshl_add_u64 v[50:51], v[50:51], 0, s[6:7]
	v_ashrrev_i32_e32 v57, 31, v56
	v_lshl_add_u32 v54, v83, 2, v54
	v_lshl_add_u64 v[50:51], v[56:57], 1, v[50:51]
	v_ashrrev_i32_e32 v55, 31, v54
	global_load_dwordx4 v[50:53], v[50:51], off
	v_lshl_add_u64 v[54:55], v[54:55], 3, s[14:15]
	global_load_dwordx4 v[60:63], v[54:55], off offset:16
	global_load_dwordx4 v[72:75], v[54:55], off
	s_mov_b64 s[6:7], 0
	s_waitcnt vmcnt(2)
	v_lshlrev_b32_e32 v54, 16, v50
	v_and_b32_e32 v50, 0xffff0000, v50
	s_waitcnt vmcnt(0)
	v_pk_mul_f32 v[76:77], v[72:73], v[50:51] op_sel:[1,0] op_sel_hi:[0,0]
	v_pk_mul_f32 v[64:65], v[72:73], v[54:55] op_sel_hi:[1,0]
	v_pk_fma_f32 v[78:79], v[72:73], v[54:55], v[76:77] op_sel_hi:[1,0,1]
	v_and_b32_e32 v54, 0xffff0000, v51
	v_lshlrev_b32_e32 v50, 16, v51
	v_pk_mul_f32 v[54:55], v[74:75], v[54:55] op_sel:[1,0] op_sel_hi:[0,0]
	v_pk_fma_f32 v[72:73], v[74:75], v[50:51], v[54:55] op_sel_hi:[1,0,1] neg_lo:[0,0,1] neg_hi:[0,0,1]
	v_pk_fma_f32 v[50:51], v[74:75], v[50:51], v[54:55] op_sel_hi:[1,0,1]
	v_sub_f32_e32 v78, v64, v76
	v_lshlrev_b32_e32 v50, 16, v52
	v_and_b32_e32 v52, 0xffff0000, v52
	v_pk_mul_f32 v[54:55], v[60:61], v[52:53] op_sel:[1,0] op_sel_hi:[0,0]
	v_pk_fma_f32 v[74:75], v[60:61], v[50:51], v[54:55] op_sel_hi:[1,0,1] neg_lo:[0,0,1] neg_hi:[0,0,1]
	v_pk_fma_f32 v[54:55], v[60:61], v[50:51], v[54:55] op_sel_hi:[1,0,1]
	v_and_b32_e32 v61, 0xffff0000, v53
	v_lshlrev_b32_e32 v60, 16, v53
	v_mul_f32_e32 v50, v63, v61
	v_pk_fma_f32 v[52:53], v[62:63], v[60:61], v[50:51] op_sel_hi:[1,1,0] neg_lo:[0,0,1] neg_hi:[0,0,1]
	v_pk_mul_f32 v[60:61], v[62:63], v[60:61] op_sel:[0,1] op_sel_hi:[1,0]
	v_mov_b32_e32 v54, v74
	v_add_f32_e32 v53, v60, v61
	v_mov_b32_e32 v50, v72

.LBB0_599:
	v_cndmask_b32_e64 v60, 1.0, v237, s[6:7]
	v_pk_mul_f32 v[56:57], v[60:61], v[78:79] op_sel_hi:[0,1]
	v_pk_mul_f32 v[50:51], v[60:61], v[50:51] op_sel_hi:[0,1]
	v_cvt_pk_bf16_f32 v56, v56, v57
	v_cvt_pk_bf16_f32 v57, v50, v51
	v_pk_mul_f32 v[50:51], v[60:61], v[54:55] op_sel_hi:[0,1]
	s_lshl_b32 s3, s4, 1
	v_cvt_pk_bf16_f32 v58, v50, v51
	v_pk_mul_f32 v[50:51], v[60:61], v[52:53] op_sel_hi:[0,1]
	s_add_u32 s3, s10, s3
	v_cvt_pk_bf16_f32 v59, v50, v51
	v_mov_b32_e32 v50, s53
	v_mov_b32_e32 v51, s82
	s_addc_u32 s5, s11, 0
	s_lshl_b32 s4, s40, 1
	v_cndmask_b32_e64 v50, v50, v51, s[6:7]
	v_mul_lo_u32 v51, v87, s69
	v_lshlrev_b32_e32 v52, 4, v89
	s_add_u32 s4, s3, s4
	v_add3_u32 v50, v50, v51, v52
	s_addc_u32 s5, s5, 0
	ds_write_b128 v50, v[56:59]
	v_add_u32_e32 v50, s20, v81
	v_mov_b64_e32 v[58:59], s[4:5]
	v_lshlrev_b32_e32 v52, 3, v82
	v_mad_i64_i32 v[50:51], s[4:5], v50, s67, v[58:59]
	v_ashrrev_i32_e32 v53, 31, v52
	v_lshl_add_u64 v[50:51], v[52:53], 1, v[50:51]
	v_add_u32_e32 v54, s20, v84
	v_lshlrev_b32_e32 v56, 3, v85
	v_mad_i64_i32 v[54:55], s[4:5], v54, s67, v[58:59]
	v_ashrrev_i32_e32 v57, 31, v56
	v_add_u32_e32 v60, s20, v87
	v_lshl_add_u64 v[54:55], v[56:57], 1, v[54:55]
	v_mad_i64_i32 v[58:59], s[4:5], v60, s67, v[58:59]
	v_lshlrev_b32_e32 v60, 3, v88
	v_ashrrev_i32_e32 v61, 31, v60
	v_lshl_add_u64 v[58:59], v[60:61], 1, v[58:59]
	v_mul_lo_u32 v62, v81, s91
	v_lshlrev_b32_e32 v63, 4, v82
	v_add3_u32 v62, s53, v62, v63
	s_movk_i32 s3, 0x380
	v_cmp_gt_i32_e32 vcc, s3, v80
	s_waitcnt vmcnt(2)
	ds_write_b128 v62, v[122:125] offset:36864
	v_mul_lo_u32 v50, v84, s91
	v_lshlrev_b32_e32 v51, 4, v85
	v_add3_u32 v50, s53, v50, v51
	v_lshlrev_b32_e32 v51, 4, v88
	s_waitcnt vmcnt(1)
	ds_write_b128 v50, v[126:129] offset:36864
	v_mul_lo_u32 v50, v87, s91
	v_add3_u32 v50, s53, v50, v51
	s_waitcnt vmcnt(0)
	ds_write_b128 v50, v[130:133] offset:36864
	s_and_saveexec_b64 s[4:5], vcc
	s_cbranch_execz .LBB0_614
	v_lshlrev_b32_e32 v50, 3, v80
	s_mov_b64 s[6:7], 0
	v_mov_b32_e32 v51, v80
	s_branch .LBB0_602

.LBB0_614:
	s_or_b64 exec, exec, s[4:5]
	s_and_b64 s[4:5], s[8:9], exec
	s_mov_b32 s3, 0x65200000
	s_cselect_b32 s3, s3, 0x67200000
	s_add_u32 s4, s76, s3
	s_addc_u32 s5, s77, 0
	s_lshl_b32 s3, s21, 3
	s_lshl_b32 s6, s97, 1
	s_movk_i32 s7, 0x480
	s_or_b32 s3, s3, s6
	v_cmp_gt_i32_e32 vcc, s7, v80
	s_and_saveexec_b64 s[12:13], vcc
	s_cbranch_execz .LBB0_616
	s_mov_b32 s7, 0x38e38e39
	v_mul_hi_i32 v50, v80, s7
	v_lshrrev_b32_e32 v51, 31, v50
	v_ashrrev_i32_e32 v50, 7, v50
	v_add_u32_e32 v50, v50, v51
	v_mul_i32_i24_e32 v51, 0x240, v50
	v_sub_u32_e32 v51, v80, v51
	v_mul_i32_i24_e32 v52, 0x2aab, v51
	v_lshrrev_b32_e32 v53, 31, v52
	v_add_u16_sdwa v54, v52, v53 dst_sel:DWORD dst_unused:UNUSED_PAD src0_sel:WORD_1 src1_sel:DWORD
	v_mul_lo_u16_e32 v52, 6, v54
	v_add_u32_e32 v50, s3, v50
	v_sub_u16_e32 v55, v51, v52
	v_lshl_or_b32 v52, v50, 6, s18
	v_mov_b64_e32 v[50:51], s[4:5]
	s_movk_i32 s7, 0x2400
	v_mad_i64_i32 v[50:51], s[14:15], v52, s7, v[50:51]
	v_mul_i32_i24_sdwa v52, sext(v54), v199 dst_sel:DWORD dst_unused:UNUSED_PAD src0_sel:WORD_0 src1_sel:DWORD
	v_ashrrev_i32_e32 v53, 31, v52
	v_lshl_add_u64 v[50:51], v[52:53], 1, v[50:51]
	v_lshlrev_b32_sdwa v52, v200, sext(v55) dst_sel:DWORD dst_unused:UNUSED_PAD src0_sel:DWORD src1_sel:WORD_0
	v_ashrrev_i32_e32 v53, 31, v52
	v_lshl_add_u64 v[50:51], v[52:53], 1, v[50:51]
	v_add_u32_e32 v56, 0x23f, v80
	s_movk_i32 s7, 0x47f
	v_mov_b32_e32 v57, s84
	v_mov_b32_e32 v58, s83
	v_cmp_gt_u32_e32 vcc, s7, v56
	v_mul_i32_i24_sdwa v54, sext(v54), s69 dst_sel:DWORD dst_unused:UNUSED_PAD src0_sel:WORD_0 src1_sel:DWORD
	v_lshlrev_b32_sdwa v55, v201, sext(v55) dst_sel:DWORD dst_unused:UNUSED_PAD src0_sel:DWORD src1_sel:WORD_0
	v_cndmask_b32_e32 v56, v57, v58, vcc
	v_add3_u32 v54, v56, v54, v55
	ds_write_b128 v54, v[108:111]
.LBB0_616:
	s_or_b64 exec, exec, s[12:13]
	s_movk_i32 s7, 0x280
	v_cmp_gt_i32_e32 vcc, s7, v80
	s_and_saveexec_b64 s[12:13], vcc
	s_cbranch_execz .LBB0_618
	s_mov_b32 s7, 0x38e38e39
	v_mul_hi_i32 v50, v83, s7
	v_lshrrev_b32_e32 v51, 31, v50
	v_ashrrev_i32_e32 v50, 7, v50
	v_add_u32_e32 v50, v50, v51
	v_mul_i32_i24_e32 v51, 0x240, v50
	v_sub_u32_e32 v51, v83, v51
	v_mul_i32_i24_e32 v52, 0x2aab, v51
	v_lshrrev_b32_e32 v53, 31, v52
	v_add_u16_sdwa v54, v52, v53 dst_sel:DWORD dst_unused:UNUSED_PAD src0_sel:WORD_1 src1_sel:DWORD
	v_mul_lo_u16_e32 v52, 6, v54
	v_add_u32_e32 v50, s3, v50
	v_sub_u16_e32 v55, v51, v52
	v_lshl_or_b32 v52, v50, 6, s18
	v_mov_b64_e32 v[50:51], s[4:5]
	s_movk_i32 s7, 0x2400
	v_mad_i64_i32 v[50:51], s[14:15], v52, s7, v[50:51]
	v_mul_i32_i24_sdwa v52, sext(v54), v199 dst_sel:DWORD dst_unused:UNUSED_PAD src0_sel:WORD_0 src1_sel:DWORD
	v_ashrrev_i32_e32 v53, 31, v52
	v_lshl_add_u64 v[50:51], v[52:53], 1, v[50:51]
	v_lshlrev_b32_sdwa v52, v200, sext(v55) dst_sel:DWORD dst_unused:UNUSED_PAD src0_sel:DWORD src1_sel:WORD_0
	v_ashrrev_i32_e32 v53, 31, v52
	v_lshl_add_u64 v[50:51], v[52:53], 1, v[50:51]
	v_add_u32_e32 v56, 0x43f, v80
	s_movk_i32 s7, 0x47f
	v_mov_b32_e32 v57, s84
	v_mov_b32_e32 v58, s83
	v_cmp_gt_u32_e32 vcc, s7, v56
	v_mul_i32_i24_sdwa v54, sext(v54), s69 dst_sel:DWORD dst_unused:UNUSED_PAD src0_sel:WORD_0 src1_sel:DWORD
	v_lshlrev_b32_sdwa v55, v201, sext(v55) dst_sel:DWORD dst_unused:UNUSED_PAD src0_sel:DWORD src1_sel:WORD_0
	v_cndmask_b32_e32 v56, v57, v58, vcc
	v_add3_u32 v54, v56, v54, v55
	ds_write_b128 v54, v[112:115]
.LBB0_618:
	s_or_b64 exec, exec, s[12:13]
	v_cmp_gt_i32_e32 vcc, s52, v80
	s_and_saveexec_b64 s[12:13], vcc
	s_cbranch_execz .LBB0_620
	s_mov_b32 s7, 0x38e38e39
	v_mul_hi_i32 v50, v86, s7
	v_lshrrev_b32_e32 v51, 31, v50
	v_ashrrev_i32_e32 v50, 7, v50
	v_add_u32_e32 v50, v50, v51
	v_mul_i32_i24_e32 v51, 0x240, v50
	v_sub_u32_e32 v51, v86, v51
	v_mul_i32_i24_e32 v52, 0x2aab, v51
	v_lshrrev_b32_e32 v53, 31, v52
	v_add_u16_sdwa v54, v52, v53 dst_sel:DWORD dst_unused:UNUSED_PAD src0_sel:WORD_1 src1_sel:DWORD
	v_mul_lo_u16_e32 v52, 6, v54
	v_add_u32_e32 v50, s3, v50
	v_sub_u16_e32 v55, v51, v52
	v_lshl_or_b32 v52, v50, 6, s18
	v_mov_b64_e32 v[50:51], s[4:5]
	s_movk_i32 s3, 0x2400
	v_mad_i64_i32 v[50:51], s[4:5], v52, s3, v[50:51]
	v_mul_i32_i24_sdwa v52, sext(v54), v199 dst_sel:DWORD dst_unused:UNUSED_PAD src0_sel:WORD_0 src1_sel:DWORD
	v_ashrrev_i32_e32 v53, 31, v52
	v_lshl_add_u64 v[50:51], v[52:53], 1, v[50:51]
	v_lshlrev_b32_sdwa v52, v200, sext(v55) dst_sel:DWORD dst_unused:UNUSED_PAD src0_sel:DWORD src1_sel:WORD_0
	v_ashrrev_i32_e32 v53, 31, v52
	v_lshl_add_u64 v[50:51], v[52:53], 1, v[50:51]
	v_add_u32_e32 v56, 0x63f, v80
	s_movk_i32 s3, 0x47f
	v_mov_b32_e32 v57, s84
	v_mov_b32_e32 v58, s83
	v_cmp_gt_u32_e32 vcc, s3, v56
	v_mul_i32_i24_sdwa v54, sext(v54), s69 dst_sel:DWORD dst_unused:UNUSED_PAD src0_sel:WORD_0 src1_sel:DWORD
	v_lshlrev_b32_sdwa v55, v201, sext(v55) dst_sel:DWORD dst_unused:UNUSED_PAD src0_sel:DWORD src1_sel:WORD_0
	v_cndmask_b32_e32 v56, v57, v58, vcc
	v_add3_u32 v54, v56, v54, v55
	ds_write_b128 v54, v[116:119]
.LBB0_620:
	s_or_b64 exec, exec, s[12:13]
	v_cndmask_b32_e64 v50, 0, 1, s[8:9]
	v_cmp_ne_u32_e64 s[4:5], 1, v50
	s_andn2_b64 vcc, exec, s[8:9]
	v_lshlrev_b32_e32 v178, 3, v175
	s_cbranch_vccnz .LBB0_622
	s_lshl_b32 s3, s19, 9
	s_lshl_b32 s7, s97, 7
	s_or_b32 s3, s3, s7
	v_lshl_add_u32 v52, v175, 1, s20
	v_mov_b64_e32 v[50:51], s[10:11]
	s_or_b32 s8, s3, s18
	s_mov_b32 s9, s41
	v_mad_i64_i32 v[50:51], s[10:11], v52, s67, v[50:51]
	s_mov_b32 s7, s41
	s_lshl_b64 s[8:9], s[8:9], 2
	v_lshl_add_u64 v[54:55], v[50:51], 0, s[6:7]
	s_add_u32 s80, s76, s8
	s_addc_u32 s81, s77, s9
	s_mov_b64 s[8:9], 0x1d00
	v_lshl_add_u64 v[52:53], v[50:51], 0, s[8:9]
	s_or_b32 s8, s6, 8
	s_mov_b32 s9, s41
	v_lshl_add_u64 v[50:51], v[52:53], 0, s[8:9]
	s_or_b32 s8, s6, 24
	v_lshl_add_u64 v[56:57], v[52:53], 0, s[8:9]
	v_and_b32_e32 v62, 64, v233
	v_add_u32_e32 v50, -1, v233
	v_add_u32_e32 v51, -2, v233
	v_cmp_lt_i32_e32 vcc, v50, v62
	v_add_u32_e32 v56, -4, v233
	s_or_b32 s8, s6, 16
	v_cndmask_b32_e32 v50, v50, v233, vcc
	v_cmp_lt_i32_e32 vcc, v51, v62
	v_lshlrev_b32_e32 v50, 2, v50
	v_cmp_gt_i32_e64 s[10:11], 2, v175
	v_cndmask_b32_e32 v51, v51, v233, vcc
	v_cmp_lt_i32_e32 vcc, v56, v62
	v_lshlrev_b32_e32 v63, 2, v51
	v_cmp_gt_i32_e64 s[16:17], 63, v175
	v_cndmask_b32_e32 v56, v56, v233, vcc
	v_lshlrev_b32_e32 v64, 2, v56
	v_lshl_add_u64 v[56:57], v[52:53], 0, s[6:7]
	v_lshl_add_u64 v[52:53], v[52:53], 0, s[8:9]
	s_nop 0
	s_nop 0
	v_cmp_gt_i32_e64 s[8:9], 1, v175
	v_cmp_gt_i32_e64 s[18:19], 62, v175
	v_cmp_gt_i32_e64 s[14:15], 16, v175
	v_cmp_gt_i32_e64 s[20:21], 60, v175
	v_cmp_gt_i32_e64 s[22:23], 56, v175
	v_cmp_gt_i32_e64 s[26:27], 48, v175
	s_waitcnt vmcnt(9)
	v_lshlrev_b32_e32 v54, 16, v138
	v_max_f32_e32 v57, v54, v54
	v_mul_f32_e64 v54, |v54|, s28
	s_waitcnt vmcnt(8)
	v_lshlrev_b32_e32 v55, 16, v139
	v_exp_f32_e32 v54, v54
	v_max_f32_e32 v58, v55, v55
	v_mul_f32_e64 v55, |v55|, s28
	v_exp_f32_e32 v55, v55
	v_add_f32_e32 v54, 1.0, v54
	s_waitcnt vmcnt(7)
	v_lshlrev_b32_e32 v59, 16, v140
	s_waitcnt vmcnt(6)
	v_lshlrev_b32_e32 v60, 16, v141
	v_max_f32_e32 v61, v59, v59
	v_mul_f32_e64 v59, |v59|, s28
	v_max_f32_e32 v65, v60, v60
	v_mul_f32_e64 v60, |v60|, s28
	v_exp_f32_e32 v59, v59
	v_exp_f32_e32 v60, v60
	v_cmp_gt_f32_e32 vcc, s55, v54
	v_add_f32_e32 v55, 1.0, v55
	v_cmp_gt_f32_e64 s[6:7], s55, v55
	v_cndmask_b32_e64 v70, 0, 32, vcc
	v_ldexp_f32 v54, v54, v70
	v_cndmask_b32_e64 v71, 0, 32, s[6:7]
	v_log_f32_e32 v54, v54
	v_add_f32_e32 v59, 1.0, v59
	v_ldexp_f32 v55, v55, v71
	v_cndmask_b32_e64 v71, 0, v232, s[6:7]
	v_add_f32_e32 v60, 1.0, v60
	v_cmp_gt_f32_e64 s[6:7], s55, v59
	v_cndmask_b32_e32 v70, 0, v232, vcc
	v_cmp_gt_f32_e32 vcc, s55, v60
	v_cndmask_b32_e64 v72, 0, 32, s[6:7]
	v_ldexp_f32 v59, v59, v72
	v_cndmask_b32_e64 v73, 0, 32, vcc
	v_ldexp_f32 v60, v60, v73
	v_mul_f32_e32 v73, 0x3f317217, v54
	v_log_f32_e32 v59, v59
	v_fma_f32 v73, v54, s94, -v73
	v_fmac_f32_e32 v73, 0x3377d1cf, v54
	v_cndmask_b32_e64 v72, 0, v232, s[6:7]
	v_fmac_f32_e32 v73, 0x3f317217, v54
	v_cmp_lt_f32_e64 s[6:7], |v54|, s95
	v_min_f32_e32 v57, 0, v57
	v_min_f32_e32 v61, 0, v61
	v_cndmask_b32_e64 v54, v54, v73, s[6:7]
	v_mul_f32_e32 v73, 0x3f317217, v59
	v_sub_f32_e32 v54, v54, v70
	v_fma_f32 v70, v59, s94, -v73
	v_fmac_f32_e32 v70, 0x3377d1cf, v59
	v_fmac_f32_e32 v70, 0x3f317217, v59
	v_cmp_lt_f32_e64 s[6:7], |v59|, s95
	v_sub_f32_e32 v57, v57, v54
	v_log_f32_e32 v55, v55
	v_cndmask_b32_e64 v54, v59, v70, s[6:7]
	v_sub_f32_e32 v54, v54, v72
	v_sub_f32_e32 v59, v61, v54
	v_add_f32_e32 v54, v57, v59
	ds_bpermute_b32 v61, v50, v54
	v_mul_f32_e32 v74, 0x3f317217, v55
	v_fma_f32 v70, v55, s94, -v74
	v_log_f32_e32 v60, v60
	v_fmac_f32_e32 v70, 0x3377d1cf, v55
	s_waitcnt lgkmcnt(0)
	v_add_f32_e32 v61, v54, v61
	v_cndmask_b32_e64 v54, v61, v54, s[8:9]
	ds_bpermute_b32 v61, v63, v54
	v_fmac_f32_e32 v70, 0x3f317217, v55
	v_cmp_lt_f32_e64 s[6:7], |v55|, s95
	v_min_f32_e32 v58, 0, v58
	v_min_f32_e32 v65, 0, v65
	s_waitcnt lgkmcnt(0)
	v_add_f32_e32 v61, v54, v61
	v_cndmask_b32_e64 v54, v61, v54, s[10:11]
	ds_bpermute_b32 v61, v64, v54
	v_cndmask_b32_e64 v55, v55, v70, s[6:7]
	v_sub_f32_e32 v55, v55, v71
	v_mul_f32_e32 v70, 0x3f317217, v60
	v_sub_f32_e32 v58, v58, v55
	s_waitcnt lgkmcnt(0)
	v_add_f32_e32 v55, v54, v61
	v_cmp_gt_i32_e64 s[6:7], 4, v175
	v_fma_f32 v70, v60, s94, -v70
	v_fmac_f32_e32 v70, 0x3377d1cf, v60
	v_cndmask_b32_e64 v54, v55, v54, s[6:7]
	v_add_u32_e32 v55, -8, v233
	v_cmp_lt_i32_e64 s[12:13], v55, v62
	v_fmac_f32_e32 v70, 0x3f317217, v60
	s_waitcnt vmcnt(3)
	v_lshlrev_b32_e32 v52, 16, v184
	v_cndmask_b32_e64 v55, v55, v233, s[12:13]
	v_cmp_lt_f32_e64 s[12:13], |v60|, s95
	v_lshlrev_b32_e32 v61, 2, v55
	ds_bpermute_b32 v55, v61, v54
	v_cndmask_b32_e64 v60, v60, v70, s[12:13]
	v_cndmask_b32_e32 v70, 0, v232, vcc
	v_sub_f32_e32 v60, v60, v70
	v_and_b32_e32 v70, 63, v233
	v_cmp_ne_u32_e64 s[12:13], 63, v70
	v_sub_f32_e32 v60, v65, v60
	v_add_f32_e32 v65, v58, v60
	v_addc_co_u32_e64 v71, s[12:13], 0, v233, s[12:13]
	v_lshlrev_b32_e32 v71, 2, v71
	ds_bpermute_b32 v72, v71, v65
	s_waitcnt lgkmcnt(1)
	v_add_f32_e32 v55, v54, v55
	v_cmp_gt_i32_e32 vcc, 8, v175
	v_cmp_gt_u32_e64 s[24:25], 48, v70
	s_waitcnt lgkmcnt(0)
	v_add_f32_e32 v72, v65, v72
	v_cndmask_b32_e32 v54, v55, v54, vcc
	v_add_u32_e32 v55, -16, v233
	v_cmp_lt_i32_e64 s[12:13], v55, v62
	v_cndmask_b32_e64 v65, v65, v72, s[16:17]
	s_nop 0
	v_cndmask_b32_e64 v55, v55, v233, s[12:13]
	v_cmp_gt_u32_e64 s[12:13], 62, v70
	v_lshlrev_b32_e32 v73, 2, v55
	ds_bpermute_b32 v55, v73, v54
	v_cndmask_b32_e64 v72, 0, 2, s[12:13]
	v_add_lshl_u32 v72, v72, v233, 2
	ds_bpermute_b32 v74, v72, v65
	v_cmp_gt_u32_e64 s[12:13], 60, v70
	s_waitcnt lgkmcnt(1)
	v_add_f32_e32 v55, v54, v55
	v_cndmask_b32_e64 v54, v55, v54, s[14:15]
	v_subrev_u32_e32 v55, 32, v233
	s_waitcnt lgkmcnt(0)
	v_add_f32_e32 v74, v65, v74
	v_cndmask_b32_e64 v65, v65, v74, s[18:19]
	v_cndmask_b32_e64 v74, 0, 4, s[12:13]
	v_add_lshl_u32 v74, v74, v233, 2
	ds_bpermute_b32 v75, v74, v65
	v_cmp_lt_i32_e64 s[12:13], v55, v62
	s_waitcnt lgkmcnt(0)
	v_add_f32_e32 v75, v65, v75
	v_cndmask_b32_e64 v55, v55, v233, s[12:13]
	v_cmp_gt_u32_e64 s[12:13], 56, v70
	v_lshlrev_b32_e32 v62, 2, v55
	v_cndmask_b32_e64 v65, v65, v75, s[20:21]
	v_cndmask_b32_e64 v75, 0, 8, s[12:13]
	ds_bpermute_b32 v55, v62, v54
	v_add_lshl_u32 v75, v75, v233, 2
	ds_bpermute_b32 v76, v75, v65
	v_cmp_gt_i32_e64 s[12:13], 32, v175
	s_waitcnt lgkmcnt(1)
	v_add_f32_e32 v55, v54, v55
	v_cndmask_b32_e64 v54, v55, v54, s[12:13]
	s_waitcnt lgkmcnt(0)
	v_add_f32_e32 v55, v65, v76
	v_cndmask_b32_e64 v65, v65, v55, s[22:23]
	v_cndmask_b32_e64 v55, 0, 16, s[24:25]
	ds_bpermute_b32 v54, v50, v54
	v_add_lshl_u32 v70, v55, v233, 2
	ds_bpermute_b32 v55, v70, v65
	v_cmp_eq_u32_e64 s[24:25], 0, v175
	s_waitcnt lgkmcnt(0)
	v_add_f32_e32 v77, v65, v55
	v_cndmask_b32_e64 v76, v54, 0, s[24:25]
	v_lshlrev_b32_e32 v55, 16, v182
	v_add_f32_e32 v56, v57, v76
	s_waitcnt vmcnt(2)
	v_lshlrev_b32_e32 v54, 16, v185
	v_add_f32_e32 v57, v59, v56
	v_pk_add_f32 v[54:55], v[54:55], v[56:57] neg_lo:[0,1] neg_hi:[0,1]
	v_mov_b32_e32 v76, 0x80
	v_max_f32_e32 v53, v54, v55
	ds_bpermute_b32 v59, v50, v53
	v_cndmask_b32_e64 v65, v65, v77, s[26:27]
	v_lshl_or_b32 v76, v233, 2, v76
	ds_bpermute_b32 v77, v76, v65
	s_waitcnt lgkmcnt(1)
	v_max_f32_e32 v59, v59, v59
	v_max_f32_e32 v59, v53, v59
	v_cndmask_b32_e64 v53, v59, v53, s[8:9]
	ds_bpermute_b32 v59, v63, v53
	s_waitcnt lgkmcnt(1)
	v_add_f32_e32 v63, v65, v77
	v_cndmask_b32_e64 v63, v65, v63, s[12:13]
	ds_bpermute_b32 v63, v71, v63
	v_cmp_eq_u32_e64 s[8:9], 63, v175
	s_waitcnt lgkmcnt(1)
	v_max_f32_e32 v59, v59, v59
	v_max_f32_e32 v59, v53, v59
	v_cndmask_b32_e64 v53, v59, v53, s[10:11]
	ds_bpermute_b32 v59, v64, v53
	s_waitcnt lgkmcnt(1)
	v_cndmask_b32_e64 v63, v63, 0, s[8:9]
	s_waitcnt lgkmcnt(0)
	v_max_f32_e32 v59, v59, v59
	v_max_f32_e32 v59, v53, v59
	v_cndmask_b32_e64 v64, v59, v53, s[6:7]
	v_add_f32_e32 v59, v60, v63
	v_lshlrev_b32_e32 v53, 16, v183
	v_add_f32_e32 v58, v58, v59
	v_pk_add_f32 v[52:53], v[52:53], v[58:59] neg_lo:[0,1] neg_hi:[0,1]
	ds_bpermute_b32 v61, v61, v64
	v_max_f32_e32 v51, v52, v53
	ds_bpermute_b32 v60, v71, v51
	s_mov_b32 s6, 0x3fb8aa3b
	s_waitcnt lgkmcnt(1)
	v_max_f32_e32 v61, v61, v61
	v_max_f32_e32 v61, v64, v61
	s_waitcnt lgkmcnt(0)
	v_max_f32_e32 v60, v60, v60
	v_max_f32_e32 v60, v51, v60
	v_cndmask_b32_e64 v51, v51, v60, s[16:17]
	ds_bpermute_b32 v60, v72, v51
	v_cndmask_b32_e32 v61, v61, v64, vcc
	ds_bpermute_b32 v63, v73, v61
	s_waitcnt lgkmcnt(1)
	v_max_f32_e32 v60, v60, v60
	v_max_f32_e32 v60, v51, v60
	v_cndmask_b32_e64 v51, v51, v60, s[18:19]
	ds_bpermute_b32 v60, v74, v51
	s_waitcnt lgkmcnt(1)
	v_max_f32_e32 v63, v63, v63
	v_max_f32_e32 v63, v61, v63
	v_cndmask_b32_e64 v61, v63, v61, s[14:15]
	ds_bpermute_b32 v62, v62, v61
	s_waitcnt lgkmcnt(1)
	v_max_f32_e32 v60, v60, v60
	v_max_f32_e32 v60, v51, v60
	v_cndmask_b32_e64 v51, v51, v60, s[20:21]
	ds_bpermute_b32 v60, v75, v51
	v_max_f32_e32 v63, v61, v61
	s_waitcnt lgkmcnt(1)
	v_max_f32_e32 v62, v62, v62
	v_max_f32_e32 v62, v63, v62
	v_cndmask_b32_e64 v61, v62, v61, s[12:13]
	s_waitcnt lgkmcnt(0)
	v_max_f32_e32 v60, v60, v60
	v_max_f32_e32 v60, v51, v60
	v_cndmask_b32_e64 v51, v51, v60, s[22:23]
	ds_bpermute_b32 v60, v70, v51
	ds_bpermute_b32 v50, v50, v61
	v_add_u32_e32 v61, s85, v178
	v_add_u32_e32 v62, s45, v178
	ds_write_b64 v61, v[56:57]
	s_waitcnt lgkmcnt(2)
	v_max_f32_e32 v60, v60, v60
	v_max_f32_e32 v60, v51, v60
	v_cndmask_b32_e64 v51, v51, v60, s[26:27]
	ds_bpermute_b32 v60, v76, v51
	s_waitcnt lgkmcnt(2)
	v_cndmask_b32_e64 v50, v50, v241, s[24:25]
	v_max_f32_e32 v50, v50, v50
	v_max_f32_e32 v63, v50, v54
	v_max_f32_e32 v50, v51, v51
	s_waitcnt lgkmcnt(0)
	v_max_f32_e32 v60, v60, v60
	v_max_f32_e32 v50, v50, v60
	v_cndmask_b32_e64 v50, v51, v50, s[12:13]
	ds_bpermute_b32 v60, v71, v50
	v_pk_mul_f32 v[50:51], v[54:55], s[6:7] op_sel_hi:[1,0]
	v_add_u32_e32 v54, s38, v178
	ds_write_b64 v54, v[50:51]
	v_max_f32_e32 v64, v63, v55
	s_waitcnt lgkmcnt(1)
	v_cndmask_b32_e64 v50, v60, v241, s[8:9]
	v_max_f32_e32 v50, v50, v50
	v_max_f32_e32 v54, v50, v53
	v_max_f32_e32 v55, v54, v52
	v_pk_mul_f32 v[50:51], v[52:53], s[6:7] op_sel_hi:[1,0]
	v_add_u32_e32 v52, s39, v178
	ds_write_b64 v52, v[50:51]
	s_waitcnt vmcnt(1)
	v_add_f32_e32 v50, v186, v56
	v_add_f32_e32 v51, v56, v63
	v_max_f32_e32 v50, v50, v51
	v_add_f32_e32 v51, v186, v57
	v_add_f32_e32 v52, v57, v64
	v_max_f32_e32 v51, v51, v52
	v_add_u32_e32 v52, s89, v178
	ds_write_b64 v52, v[50:51]
	s_waitcnt vmcnt(0)
	v_add_f32_e32 v50, v187, v58
	v_add_f32_e32 v51, v58, v55
	v_max_f32_e32 v50, v50, v51
	v_add_f32_e32 v51, v187, v59
	v_add_f32_e32 v52, v59, v54
	v_max_f32_e32 v51, v51, v52
	v_add_u32_e32 v52, s54, v178
	ds_write_b64 v62, v[58:59]
	ds_write_b64 v52, v[50:51]
	v_mov_b32_e32 v180, v186
	v_mov_b32_e32 v181, v187
	s_branch .LBB0_623

	.amdhsa_kernel _Z10hybrid_fwdILi1023EEv4Args
		.amdhsa_group_segment_fixed_size 0
		.amdhsa_private_segment_fixed_size 0
		.amdhsa_kernarg_size 432
		.amdhsa_user_sgpr_count 2
		.amdhsa_user_sgpr_dispatch_ptr 0
		.amdhsa_user_sgpr_queue_ptr 0
		.amdhsa_user_sgpr_kernarg_segment_ptr 1
		.amdhsa_user_sgpr_dispatch_id 0
		.amdhsa_user_sgpr_kernarg_preload_length 0
		.amdhsa_user_sgpr_kernarg_preload_offset 0
		.amdhsa_user_sgpr_private_segment_size 0
		.amdhsa_uses_dynamic_stack 0
		.amdhsa_enable_private_segment 0
		.amdhsa_system_sgpr_workgroup_id_x 1
		.amdhsa_system_sgpr_workgroup_id_y 0
		.amdhsa_system_sgpr_workgroup_id_z 0
		.amdhsa_system_sgpr_workgroup_info 0
		.amdhsa_system_vgpr_workitem_id 0
		.amdhsa_next_free_vgpr 256
		.amdhsa_next_free_sgpr 102
		.amdhsa_accum_offset 256
		.amdhsa_reserve_vcc 1
		.amdhsa_float_round_mode_32 0
		.amdhsa_float_round_mode_16_64 0
		.amdhsa_float_denorm_mode_32 3
		.amdhsa_float_denorm_mode_16_64 3
		.amdhsa_dx10_clamp 1
		.amdhsa_ieee_mode 1
		.amdhsa_fp16_overflow 0
		.amdhsa_tg_split 0
		.amdhsa_exception_fp_ieee_invalid_op 0
		.amdhsa_exception_fp_denorm_src 0
		.amdhsa_exception_fp_ieee_div_zero 0
		.amdhsa_exception_fp_ieee_overflow 0
		.amdhsa_exception_fp_ieee_underflow 0
		.amdhsa_exception_fp_ieee_inexact 0
		.amdhsa_exception_int_div_zero 0
	.end_amdhsa_kernel

amdhsa.kernels:
  - .agpr_count:     0
    .args:
      - .offset:         0
        .size:           176
        .value_kind:     by_value
      - .offset:         176
        .size:           4
        .value_kind:     hidden_block_count_x
      - .offset:         180
        .size:           4
        .value_kind:     hidden_block_count_y
      - .offset:         184
        .size:           4
        .value_kind:     hidden_block_count_z
      - .offset:         188
        .size:           2
        .value_kind:     hidden_group_size_x
      - .offset:         190
        .size:           2
        .value_kind:     hidden_group_size_y
      - .offset:         192
        .size:           2
        .value_kind:     hidden_group_size_z
      - .offset:         194
        .size:           2
        .value_kind:     hidden_remainder_x
      - .offset:         196
        .size:           2
        .value_kind:     hidden_remainder_y
      - .offset:         198
        .size:           2
        .value_kind:     hidden_remainder_z
      - .offset:         216
        .size:           8
        .value_kind:     hidden_global_offset_x
      - .offset:         224
        .size:           8
        .value_kind:     hidden_global_offset_y
      - .offset:         232
        .size:           8
        .value_kind:     hidden_global_offset_z
      - .offset:         240
        .size:           2
        .value_kind:     hidden_grid_dims
      - .offset:         296
        .size:           4
        .value_kind:     hidden_dynamic_lds_size
    .group_segment_fixed_size: 0
    .kernarg_segment_align: 8
    .kernarg_segment_size: 432
    .language:       OpenCL C
    .language_version:
      - 2
      - 0
    .max_flat_workgroup_size: 512
    .name:           _Z10hybrid_fwdILi1023EEv4Args
    .private_segment_fixed_size: 0
    .sgpr_count:     108
    .sgpr_spill_count: 12
    .symbol:         _Z10hybrid_fwdILi1023EEv4Args.kd
    .uniform_work_group_size: 1
    .uses_dynamic_stack: false
    .vgpr_count:     256
    .vgpr_spill_count: 0
    .wavefront_size: 64
